# speedup vs baseline: 1.0259x; 1.0074x over previous
.Lfl0_skip:
	v_add_u32_e32 v250, v110, v226
	s_nop 1
	v_accvgpr_read_b32 v10, a128
	v_accvgpr_read_b32 v11, a129
	v_accvgpr_read_b32 v12, a130
	v_accvgpr_read_b32 v13, a131
	v_cvt_pk_f16_f32 v1, v12, v13
	v_cvt_pk_f16_f32 v0, v10, v11
	v_accvgpr_read_b32 v6, a132
	v_accvgpr_read_b32 v7, a133
	v_accvgpr_read_b32 v8, a134
	v_accvgpr_read_b32 v9, a135
	v_cvt_pk_f16_f32 v3, v8, v9
	v_cvt_pk_f16_f32 v2, v6, v7
	ds_write2_b64 v221, v[0:1], v[2:3] offset0:48 offset1:80
	s_cmp_lt_u32 s25, 12
	s_cbranch_scc0 .Lmd_dec
	s_branch .Lst1_entry
